# tail-fill at two sites: in-proj 4th round (Q=6) and layer-0 down-GEMM half round (Q=5); attention quotas 20/18 + balance
# speedup vs baseline: 1.0173x; 1.0045x over previous
; #define LAS __attribute__((address_space(3)))
; __global__ void __launch_bounds__(512, 2) mk_fwd(Args a) {
;     extern __shared__ __attribute__((aligned(16))) unsigned char lds_raw[];
;     Ctx c; c.lds = (LAS unsigned char*)lds_raw; c.tid = threadIdx.x; c.lane = c.tid & 63; c.wave = __builtin_amdgcn_readfirstlane(c.tid >> 6); c.bid = blockIdx.x; c.G = gridDim.x;
;     volatile LAS unsigned* MISC = (volatile LAS unsigned*)(c.lds + LDS_MISC);
;     if (c.tid < 32) MISC[c.tid] = 0u;
;     __syncthreads();
;     XcdBarrier bar; bar.bar = (unsigned*)(a.ws + WS_CTL) + 4096; bar.x = 0; bar.st = nullptr;
;     const int lo = a.ph_lo, hi = a.ph_hi;
;     if (hi - lo > 1) bar = xcd_barrier_post((unsigned*)(a.ws + WS_CTL) + 4096, MISC + 8);
_Z6mk_fwd4Args:
	v_writelane_b32 v255, 0, 43
	v_writelane_b32 v255, 0, 42
	s_mov_b64 s[36:37], s[0:1]
	s_load_dword s91, s[0:1], 0xf0
	s_add_u32 s0, s36, 0xf0
	s_addc_u32 s1, s37, 0
	s_mov_b32 s90, s2
	v_writelane_b32 v252, s0, 0
	v_cmp_gt_u32_e32 vcc, 32, v0
	s_nop 0
	v_writelane_b32 v252, s1, 1
	s_and_saveexec_b64 s[0:1], vcc
	v_lshl_add_u32 v1, v0, 2, 0
	v_add_u32_e32 v1, 0x27000, v1
	v_mov_b32_e32 v2, 0
	ds_write_b32 v1, v2
	s_or_b64 exec, exec, s[0:1]
	s_load_dwordx4 s[68:71], s[36:37], 0xe0
	s_mov_b32 s33, 0
	v_cmp_eq_u32_e32 vcc, 0, v0
	s_waitcnt lgkmcnt(0)
	s_barrier
	s_add_u32 s0, s68, 0x4000
	s_addc_u32 s1, s69, 0
	s_sub_i32 s2, s71, s70
	v_writelane_b32 v252, s0, 2
	s_cmp_gt_i32 s2, 1
	s_nop 0
	v_writelane_b32 v252, s1, 3
	s_cselect_b64 s[0:1], -1, 0
	s_cmp_lt_i32 s2, 2
	s_mov_b32 s2, 0
	v_writelane_b32 v252, s2, 4
	s_cbranch_scc1 .LBB0_8
	s_getreg_b32 s2, hwreg(HW_REG_XCC_ID, 0, 4)
	s_and_b32 s33, s2, 15
	s_and_saveexec_b64 s[2:3], vcc
	s_cbranch_execz .LBB0_7
	s_mov_b64 s[6:7], exec
	v_mbcnt_lo_u32_b32 v1, s6, 0
	v_mbcnt_hi_u32_b32 v1, s7, v1
	v_cmp_eq_u32_e32 vcc, 0, v1
	s_and_saveexec_b64 s[4:5], vcc
	s_cbranch_execz .LBB0_6
	s_bcnt1_i32_b64 s6, s[6:7]
	s_lshl_b32 s8, s33, 8
	v_mov_b32_e32 v3, s6
	v_readlane_b32 s6, v252, 2
	v_mov_b32_e32 v2, s8
	v_readlane_b32 s7, v252, 3
	s_nop 4
	global_atomic_add v2, v2, v3, s[6:7] offset:1024 sc0

; __global__ void __launch_bounds__(512, 2) mk_fwd(Args a) {
;     ...
;         if (IN(pb + 5) && (c.bid & 1) == 0) { if (l == 0) mod_items(a, c, 1); bg_take(a, c, l == 0 ? 26 : 24); }
;         if (EN(5) && IN(pb + 5)) for (int rep = 0; rep < NREP(5); ++rep) { phase_attn(a, c, l, last); }
;         if (IN(pb + 5) && (c.bid & 1) == 1) { bg_take(a, c, l == 0 ? 26 : 24); if (l == 0) mod_items(a, c, 1); }
.Lbal1_l1:
	s_mov_b32 s14, 18

; #define GAS __attribute__((address_space(1)))
; #define WSW(T, off, l) WSP(T, WS_WSET + (size_t)(l) * WSET_STRIDE + (off))
; #define SEAM(k) do { if (IN(k) && IN((k) + 1)) { XcdBarrier b_ = bar; { GAS unsigned* t_ = (GAS unsigned*)b_.bar; asm volatile("" : "+s"(t_)); b_.bar = (unsigned*)t_; } xcd_barrier(b_); } } while (0)
; __device__ __forceinline__ void bg_take(const Args& a, const Ctx& c0, int n) {
;     ...
;         __syncthreads();
;     }
;     __syncthreads();
; __global__ void __launch_bounds__(512, 2) mk_fwd(Args a) {
;     ...
;         if (EN(10) && IN(pb + 10)) for (int rep = 0; rep < NREP(10); ++rep) {
;             GAS unsigned char* wsb = (GAS unsigned char*)a.ws; asm volatile("" : "+s"(wsb));
;             ProbDown p; p.K = DM; p.lda = DM; p.ldb = DM; p.tpe = last ? 8 : 9; p.ord.init(NE * p.tpe, 8, c.G, c.bid, p.tpe); p.ACT = (const char*)WSP(unsigned char, WS_ACT); p.Bt = (const char*)WSW(unsigned char, W_DN, l); p.YE = WSP(bf16, WS_YE); p.gatev = WSP(const float, WS_GATEV);
;             pg8::gemm_phase(c.lds, p); }
;     ...
;         if (IN(pb + 10) && l == 0) bg_fill(a, c, 6, 0);
;     ...
;         SEAM(pb + 10);
.Lbt1_notA:
	v_readlane_b32 s2, v255, 43
	s_nop 3
	s_cmp_eq_u32 s2, 1
	s_cbranch_scc0 .Lbt1_notB
	v_writelane_b32 v255, 2, 43
	s_branch .Ltramp_back

; __global__ void __launch_bounds__(512, 2) mk_fwd(Args a) {
;     ...
;         if (IN(pb + 5) && (c.bid & 1) == 0) { if (l == 0) mod_items(a, c, 1); bg_take(a, c, l == 0 ? 26 : 24); }
;         if (EN(5) && IN(pb + 5)) for (int rep = 0; rep < NREP(5); ++rep) { phase_attn(a, c, l, last); }
;         if (IN(pb + 5) && (c.bid & 1) == 1) { bg_take(a, c, l == 0 ? 26 : 24); if (l == 0) mod_items(a, c, 1); }
.Lbal2_l1:
	s_mov_b32 s10, 18

; __device__ __forceinline__ unsigned pk2(float lo, float hi) { return f2bf(lo) | (f2bf(hi) << 16); }
; #define PG8_BAR __builtin_amdgcn_s_barrier()
; template <class P>
; __device__ __forceinline__ void gemm_phase(LAS unsigned char* lds, const P& p) {
;     ...
;         if (!has_next) break;
; #pragma unroll
;         for (int a = 0; a < 2; ++a)
; #pragma unroll
;             for (int b = 0; b < 2; ++b)
; #pragma unroll
;                 for (int m = 0; m < 4; ++m)
; #pragma unroll
;                     for (int n = 0; n < 2; ++n) acc[a][b][m][n] = (f32x4){0.f, 0.f, 0.f, 0.f};
;         cur = nxt; cA = nA; cB = nB; ++ui;
;         if (wr == 1) PG8_BAR;
;     __device__ __forceinline__ void epi(const f32x4 (&acc)[2][2][4][2], const Unit& u, int wr, int wc, int fr, int fq) const {
;     ...
;                     const f32x4 o0 = x0 + g0 * acc[ai][bj][m][0], o1 = x1v + g1v * acc[ai][bj][m][1];
;                     u32x4 ow; ow.x = pk2(o0[0], o0[1]); ow.y = pk2(o0[2], o0[3]); ow.z = pk2(o1[0], o1[1]); ow.w = pk2(o1[2], o1[3]);
;                     *(u32x4*)(xo + (ro + cofs) * 2 + loff2) = ow; }
.LBB0_1824:
	s_waitcnt vmcnt(0)
	v_pk_fma_f32 v[6:7], v[6:7], v[14:15], v[22:23]
	v_pk_fma_f32 v[12:13], v[4:5], v[12:13], v[20:21]
	v_pk_fma_f32 v[4:5], v[2:3], v[10:11], v[18:19]
	v_pk_fma_f32 v[8:9], v[8:9], v[16:17], v[24:25]
	v_cvt_pk_bf16_f32 v2, v6, v7
	v_cvt_pk_bf16_f32 v3, v8, v9
	v_bfe_u32 v1, v4, 16, 1
	v_add3_u32 v1, v4, v1, s37
	v_bfe_u32 v4, v5, 16, 1
	v_lshrrev_b32_e32 v1, 16, v1
	v_add3_u32 v4, v5, v4, s37
	v_and_or_b32 v4, v4, s33, v1
	v_add_co_u32_e32 v6, vcc, 0xb0000, v160
	v_cvt_pk_bf16_f32 v5, v12, v13
	s_nop 0
	v_addc_co_u32_e32 v7, vcc, 0, v161, vcc
	global_store_dwordx4 v[6:7], v[2:5], off offset:256
	s_andn2_b64 vcc, exec, s[38:39]
	s_mov_b64 s[24:25], -1
	s_cbranch_vccnz .LBB0_1761
	s_andn2_b64 vcc, exec, s[4:5]
	s_cbranch_vccnz .LBB0_1760
	s_barrier
	s_branch .LBB0_1760
.Ltramp_fwd:
	s_branch .Lbt1_entry
.Ltramp_back:
	s_branch .LBB0_2672
.LBB0_1827:
	v_mov_b32_e32 v129, 0
	v_mov_b32_e32 v128, v129
	v_mov_b32_e32 v127, v129
	v_mov_b32_e32 v126, v129
	v_mov_b32_e32 v125, v129
	v_mov_b32_e32 v124, v129
	v_mov_b32_e32 v123, v129
	v_mov_b32_e32 v122, v129
	v_mov_b32_e32 v113, v129
	v_mov_b32_e32 v112, v129
	v_mov_b32_e32 v111, v129
	v_mov_b32_e32 v110, v129
	v_mov_b32_e32 v109, v129
	v_mov_b32_e32 v108, v129
	v_mov_b32_e32 v107, v129
	v_mov_b32_e32 v106, v129
	v_mov_b32_e32 v97, v129
	v_mov_b32_e32 v96, v129
	v_mov_b32_e32 v95, v129
	v_mov_b32_e32 v94, v129
	v_mov_b32_e32 v93, v129
	v_mov_b32_e32 v92, v129
	v_mov_b32_e32 v91, v129
	v_mov_b32_e32 v90, v129
	v_mov_b32_e32 v81, v129
	v_mov_b32_e32 v80, v129
	v_mov_b32_e32 v79, v129
	v_mov_b32_e32 v78, v129
	v_mov_b32_e32 v77, v129
	v_mov_b32_e32 v76, v129
	v_mov_b32_e32 v75, v129
	v_mov_b32_e32 v74, v129
	v_mov_b32_e32 v121, v129
	v_mov_b32_e32 v120, v129
	v_mov_b32_e32 v119, v129
	v_mov_b32_e32 v118, v129
	v_mov_b32_e32 v117, v129
	v_mov_b32_e32 v116, v129
	v_mov_b32_e32 v115, v129
	v_mov_b32_e32 v114, v129
	v_mov_b32_e32 v105, v129
	v_mov_b32_e32 v104, v129
	v_mov_b32_e32 v103, v129
	v_mov_b32_e32 v102, v129
	v_mov_b32_e32 v101, v129
	v_mov_b32_e32 v100, v129
	v_mov_b32_e32 v99, v129
	v_mov_b32_e32 v98, v129
	v_mov_b32_e32 v89, v129
	v_mov_b32_e32 v88, v129
	v_mov_b32_e32 v87, v129
	v_mov_b32_e32 v86, v129
	v_mov_b32_e32 v85, v129
	v_mov_b32_e32 v84, v129
	v_mov_b32_e32 v83, v129
	v_mov_b32_e32 v82, v129
	v_mov_b32_e32 v73, v129
	v_mov_b32_e32 v72, v129
	v_mov_b32_e32 v71, v129
	v_mov_b32_e32 v70, v129
	v_mov_b32_e32 v69, v129
	v_mov_b32_e32 v68, v129
	v_mov_b32_e32 v67, v129
	v_mov_b32_e32 v66, v129
	v_mov_b32_e32 v65, v129
	v_mov_b32_e32 v64, v129
	v_mov_b32_e32 v63, v129
	v_mov_b32_e32 v62, v129
	v_mov_b32_e32 v61, v129
	v_mov_b32_e32 v60, v129
	v_mov_b32_e32 v59, v129
	v_mov_b32_e32 v58, v129
	v_mov_b32_e32 v49, v129
	v_mov_b32_e32 v48, v129
	v_mov_b32_e32 v47, v129
	v_mov_b32_e32 v46, v129
	v_mov_b32_e32 v45, v129
	v_mov_b32_e32 v44, v129
	v_mov_b32_e32 v43, v129
	v_mov_b32_e32 v42, v129
	v_mov_b32_e32 v33, v129
	v_mov_b32_e32 v32, v129
	v_mov_b32_e32 v31, v129
	v_mov_b32_e32 v30, v129
	v_mov_b32_e32 v29, v129
	v_mov_b32_e32 v28, v129
	v_mov_b32_e32 v27, v129
	v_mov_b32_e32 v26, v129
	v_mov_b32_e32 v17, v129
	v_mov_b32_e32 v16, v129
	v_mov_b32_e32 v15, v129
	v_mov_b32_e32 v14, v129
	v_mov_b32_e32 v13, v129
	v_mov_b32_e32 v12, v129
	v_mov_b32_e32 v11, v129
	v_mov_b32_e32 v10, v129
	v_mov_b32_e32 v57, v129
	v_mov_b32_e32 v56, v129
	v_mov_b32_e32 v55, v129
	v_mov_b32_e32 v54, v129
	v_mov_b32_e32 v53, v129
	v_mov_b32_e32 v52, v129
	v_mov_b32_e32 v51, v129
	v_mov_b32_e32 v50, v129
	v_mov_b32_e32 v41, v129
	v_mov_b32_e32 v40, v129
	v_mov_b32_e32 v39, v129
	v_mov_b32_e32 v38, v129
	v_mov_b32_e32 v37, v129
	v_mov_b32_e32 v36, v129
	v_mov_b32_e32 v35, v129
	v_mov_b32_e32 v34, v129
	v_mov_b32_e32 v25, v129
	v_mov_b32_e32 v24, v129
	v_mov_b32_e32 v23, v129
	v_mov_b32_e32 v22, v129
	v_mov_b32_e32 v21, v129
	v_mov_b32_e32 v20, v129
	v_mov_b32_e32 v19, v129
	v_mov_b32_e32 v18, v129
	v_mov_b32_e32 v9, v129
	v_mov_b32_e32 v8, v129
	v_mov_b32_e32 v7, v129
	v_mov_b32_e32 v6, v129
	v_mov_b32_e32 v5, v129
	v_mov_b32_e32 v4, v129
	v_mov_b32_e32 v3, v129
	v_mov_b32_e32 v2, v129
	s_and_b64 vcc, exec, s[14:15]
	s_cbranch_vccnz .LBB0_1768
	s_branch .LBB0_1769

; #define GAS __attribute__((address_space(1)))
; #define WSW(T, off, l) WSP(T, WS_WSET + (size_t)(l) * WSET_STRIDE + (off))
; #define SEAM(k) do { if (IN(k) && IN((k) + 1)) { XcdBarrier b_ = bar; { GAS unsigned* t_ = (GAS unsigned*)b_.bar; asm volatile("" : "+s"(t_)); b_.bar = (unsigned*)t_; } xcd_barrier(b_); } } while (0)
; __global__ void __launch_bounds__(512, 2) mk_fwd(Args a) {
;     ...
;         if (EN(10) && IN(pb + 10)) for (int rep = 0; rep < NREP(10); ++rep) {
;             GAS unsigned char* wsb = (GAS unsigned char*)a.ws; asm volatile("" : "+s"(wsb));
;             ProbDown p; p.K = DM; p.lda = DM; p.ldb = DM; p.tpe = last ? 8 : 9; p.ord.init(NE * p.tpe, 8, c.G, c.bid, p.tpe); p.ACT = (const char*)WSP(unsigned char, WS_ACT); p.Bt = (const char*)WSW(unsigned char, W_DN, l); p.YE = WSP(bf16, WS_YE); p.gatev = WSP(const float, WS_GATEV);
;             pg8::gemm_phase(c.lds, p); }
;     ...
;         if (IN(pb + 10) && l == 0) bg_fill(a, c, 6, 0);
;     ...
;         SEAM(pb + 10);
.LBB0_2673:
	v_readlane_b32 s2, v255, 43
	s_nop 3
	s_cmp_lg_u32 s2, 0
	s_cbranch_scc1 .LtailB_ret
	s_cmp_lt_u32 s90, 128
	s_cbranch_scc1 .LtailB_cont
	v_readlane_b32 s3, v254, 17
	s_nop 3
	s_cmp_lg_u32 s3, 0
	s_cbranch_scc1 .LtailB_cont
	v_writelane_b32 v255, 1, 43
	s_mov_b32 s30, 0xc3e00000
	s_movk_i32 s78, 0x315c
	v_readlane_b32 s76, v254, 53
	s_mov_b32 s81, 0x10000
	s_mov_b32 s82, 0x18000
	s_mov_b32 s83, 0x8000
	s_mov_b32 s86, 0xc000
	s_mov_b32 s14, 5
	s_branch .Ltramp_fwd
.LtailB_ret:
	v_writelane_b32 v255, 0, 43
	s_mov_b64 s[20:21], 0x2000
